# router-phase hosting: idle workgroups of E(0)/E(1) convert layer-1 down items [0xa800,0xc000); pool-1 end shrunk to 0xa800
# speedup vs baseline: 1.0033x; 1.0006x over previous
; #pragma unroll
;     for (int e = 0; e < 32; ++e) t += (cnt[e] + 255) >> 8;
;     return t; }
; __device__ __forceinline__ void side_range(const Params& p, int layer, int beg, int end, int first, int stride) {
;     const int lane = otid() & 63;
; #pragma unroll 1
;     for (int it0 = beg + first; it0 < end; it0 += 2 * stride) {
;         f32x4 v0[8], v1[8]; const int it1 = it0 + stride; const bool two = it1 < end;
;         moe_item_copy_nt(p, layer, it0, lane, v0, false); if (two) moe_item_copy_nt(p, layer, it1, lane, v1, false);
;         moe_item_copy_nt(p, layer, it0, lane, v0, true); if (two) moe_item_copy_nt(p, layer, it1, lane, v1, true);
;     }
; }
; __device__ __forceinline__ PoolRanges pool_ranges(const Params& p, int L) {
;     const int T = moe_tiles((const int*)(p.ws + ws::CTL) + ws::CW_CNT + L * 32);
;     PoolRanges r; r.rem_up = (8 * T) & 255; r.ns_up = r.rem_up ? 256 - r.rem_up : 0; r.rem_dn = T & 63; r.ns_dn = r.rem_dn ? (64 - r.rem_dn) * 4 : 0;
;     r.beg_up = L == 0 ? POOL1_BEG : (L == 1 ? POOL2_BEG : POOL3_BEG); r.pool_end = L == 0 ? 49152 : (L == 1 ? POOL2_END : POOL3_END);
;     r.end_up = min(r.beg_up + r.ns_up * 8 * SIDE_JU, r.pool_end); r.end_dn = min(r.end_up + r.ns_dn * 8 * SIDE_JU, r.pool_end);
;     return r;
; }
; __device__ __forceinline__ void moe_up_tail(const Params& p, int L, int bid) {
;     const PoolRanges r = pool_ranges(p, L);
;     if (r.ns_up && bid >= r.rem_up) side_range(p, L + 1, r.beg_up, r.end_up, (bid - r.rem_up) * 8 + (otid() >> 6), r.ns_up * 8);
; }
; __device__ __forceinline__ void moe_down_tail(const Params& p, int L, int bid) {
;     const PoolRanges r = pool_ranges(p, L); const int j = bid >> 3, tl = (bid & 7) * 8 + (j >> 2);
;     if (r.ns_dn && tl >= r.rem_dn) side_range(p, L + 1, r.end_up, r.end_dn, ((tl - r.rem_dn) * 4 + (j & 3)) * 8 + (otid() >> 6), r.ns_dn * 8);
; }
; __device__ __forceinline__ void moe_pool_finish(const Params& p, int L, int bid, int nb) {
;     const PoolRanges r = pool_ranges(p, L);
;     side_range(p, L + 1, r.end_dn, r.pool_end, bid * 8 + (otid() >> 6), nb * 8);
; }
; __global__ void __launch_bounds__(NTHR, 2) mega(Params p) {
;     ...
;         const int pb = 1 + 9 * layer;
;         if (PH(pb + 0)) { if (layer == 1 && nb == 256) moe_pool_finish(p, 0, bid, nb); if (layer == 3 && nb == 256) moe_pool_finish(p, 2, bid, nb); phaseA(p, layer, lds, bid, nb); }
.LBB0_140:
	s_mov_b32 s0, s4
	v_writelane_b32 v255, s0, 8
	v_readlane_b32 s6, v249, 0
	v_readlane_b32 s7, v249, 1
	v_writelane_b32 v255, s1, 9
	s_mul_i32 s0, s4, 9
	s_add_i32 s4, s0, 1
	s_cmp_lt_i32 s4, s6
	v_writelane_b32 v255, s0, 10
	s_cselect_b64 s[0:1], -1, 0
	s_cmp_ge_i32 s4, s7
	s_cselect_b64 s[4:5], -1, 0
	s_or_b64 s[0:1], s[0:1], s[4:5]
	s_and_b64 vcc, exec, s[0:1]
	s_cbranch_vccnz .LBB0_227
	v_readlane_b32 s0, v255, 8
	v_readlane_b32 s1, v255, 9
	s_cmp_lg_u32 s0, 1
	v_readlane_b32 s4, v254, 58
	s_cselect_b64 s[0:1], -1, 0
	v_readlane_b32 s5, v254, 59
	s_or_b64 s[0:1], s[4:5], s[0:1]
	v_readlane_b32 s20, v250, 4
	s_and_b64 vcc, exec, s[0:1]
	v_readlane_b32 s21, v250, 5
	s_cbranch_vccnz .LBB0_166
	v_readlane_b32 s0, v249, 56
	v_readlane_b32 s1, v249, 57
	s_waitcnt lgkmcnt(0)
	s_nop 3
	global_load_dwordx4 v[4:7], v3, s[0:1]
	global_load_dwordx4 v[8:11], v3, s[0:1] offset:16
	global_load_dwordx4 v[12:15], v3, s[0:1] offset:32
	global_load_dwordx4 v[16:19], v3, s[0:1] offset:48
	v_readlane_b32 s0, v249, 58
	v_readlane_b32 s1, v249, 59
	s_nop 4
	global_load_dwordx4 v[20:23], v3, s[0:1]
	global_load_dwordx4 v[24:27], v3, s[0:1] offset:16
	global_load_dwordx4 v[28:31], v3, s[0:1] offset:32
	global_load_dwordx4 v[32:35], v3, s[0:1] offset:48
	v_mov_b32_e32 v1, v0
	s_movk_i32 s0, 0x60
	v_ashrrev_i32_e32 v2, 6, v1
	s_waitcnt vmcnt(0)
	v_add_u32_e32 v1, 0xff, v4
	v_add_u32_e32 v4, 0xff, v5
	v_add_u32_e32 v5, 0xff, v6
	v_ashrrev_i32_e32 v1, 8, v1
	v_ashrrev_i32_e32 v4, 8, v4
	v_add_u32_e32 v6, 0xff, v7
	v_ashrrev_i32_e32 v5, 8, v5
	v_add_u32_e32 v1, v4, v1
	s_waitcnt vmcnt(6)
	v_add_u32_e32 v7, 0xff, v8
	v_ashrrev_i32_e32 v6, 8, v6
	v_add_u32_e32 v1, v1, v5
	v_add_u32_e32 v8, 0xff, v9
	v_ashrrev_i32_e32 v7, 8, v7
	v_add_u32_e32 v1, v1, v6
	v_add_u32_e32 v9, 0xff, v10
	v_ashrrev_i32_e32 v8, 8, v8
	v_add_u32_e32 v1, v1, v7
	v_add_u32_e32 v10, 0xff, v11
	v_ashrrev_i32_e32 v9, 8, v9
	v_add_u32_e32 v1, v1, v8
	s_waitcnt vmcnt(5)
	v_add_u32_e32 v11, 0xff, v12
	v_ashrrev_i32_e32 v10, 8, v10
	v_add_u32_e32 v1, v1, v9
	v_add_u32_e32 v12, 0xff, v13
	v_ashrrev_i32_e32 v11, 8, v11
	v_add_u32_e32 v1, v1, v10
	v_add_u32_e32 v13, 0xff, v14
	v_ashrrev_i32_e32 v12, 8, v12
	v_add_u32_e32 v1, v1, v11
	v_add_u32_e32 v14, 0xff, v15
	v_ashrrev_i32_e32 v13, 8, v13
	v_add_u32_e32 v1, v1, v12
	s_waitcnt vmcnt(4)
	v_add_u32_e32 v15, 0xff, v16
	v_ashrrev_i32_e32 v14, 8, v14
	v_add_u32_e32 v1, v1, v13
	v_add_u32_e32 v16, 0xff, v17
	v_ashrrev_i32_e32 v15, 8, v15
	v_add_u32_e32 v1, v1, v14
	v_add_u32_e32 v17, 0xff, v18
	v_ashrrev_i32_e32 v16, 8, v16
	v_add_u32_e32 v1, v1, v15
	v_add_u32_e32 v18, 0xff, v19
	v_ashrrev_i32_e32 v17, 8, v17
	v_add_u32_e32 v1, v1, v16
	s_waitcnt vmcnt(3)
	v_add_u32_e32 v19, 0xff, v20
	v_ashrrev_i32_e32 v18, 8, v18
	v_add_u32_e32 v1, v1, v17
	v_add_u32_e32 v20, 0xff, v21
	v_ashrrev_i32_e32 v19, 8, v19
	v_add_u32_e32 v1, v1, v18
	v_add_u32_e32 v21, 0xff, v22
	v_ashrrev_i32_e32 v20, 8, v20
	v_add_u32_e32 v1, v1, v19
	v_add_u32_e32 v22, 0xff, v23
	v_ashrrev_i32_e32 v21, 8, v21
	v_add_u32_e32 v1, v1, v20
	s_waitcnt vmcnt(2)
	v_add_u32_e32 v23, 0xff, v24
	v_ashrrev_i32_e32 v22, 8, v22
	v_add_u32_e32 v1, v1, v21
	v_add_u32_e32 v24, 0xff, v25
	v_ashrrev_i32_e32 v23, 8, v23
	v_add_u32_e32 v1, v1, v22
	v_add_u32_e32 v25, 0xff, v26
	v_ashrrev_i32_e32 v24, 8, v24
	v_add_u32_e32 v1, v1, v23
	v_add_u32_e32 v26, 0xff, v27
	v_ashrrev_i32_e32 v25, 8, v25
	v_add_u32_e32 v1, v1, v24
	s_waitcnt vmcnt(1)
	v_add_u32_e32 v27, 0xff, v28
	v_ashrrev_i32_e32 v26, 8, v26
	v_add_u32_e32 v1, v1, v25
	v_add_u32_e32 v28, 0xff, v29
	v_ashrrev_i32_e32 v27, 8, v27
	v_add_u32_e32 v1, v1, v26
	v_add_u32_e32 v29, 0xff, v30
	v_ashrrev_i32_e32 v28, 8, v28
	v_add_u32_e32 v1, v1, v27
	v_add_u32_e32 v30, 0xff, v31
	v_ashrrev_i32_e32 v29, 8, v29
	v_add_u32_e32 v1, v1, v28
	s_waitcnt vmcnt(0)
	v_add_u32_e32 v31, 0xff, v32
	v_ashrrev_i32_e32 v30, 8, v30
	v_add_u32_e32 v1, v1, v29
	v_add_u32_e32 v32, 0xff, v33
	v_ashrrev_i32_e32 v31, 8, v31
	v_add_u32_e32 v1, v1, v30
	v_add_u32_e32 v33, 0xff, v34
	v_ashrrev_i32_e32 v32, 8, v32
	v_add_u32_e32 v1, v1, v31
	v_add_u32_e32 v34, 0xff, v35
	v_ashrrev_i32_e32 v33, 8, v33
	v_add_u32_e32 v1, v1, v32
	v_ashrrev_i32_e32 v34, 8, v34
	v_add_u32_e32 v1, v1, v33
	v_add_u32_e32 v1, v1, v34
	v_and_b32_e32 v4, 63, v1
	v_lshlrev_b32_e32 v1, 3, v1
	v_lshlrev_b32_e32 v5, 2, v4
	v_and_b32_e32 v1, 0xf8, v1
	v_sub_u32_e32 v5, 0x100, v5
	v_sub_u32_e32 v6, 0x100, v1
	v_mul_lo_u32 v6, v6, s0
	v_mul_lo_u32 v5, v5, s0
	v_cmp_ne_u32_e32 vcc, 0, v4
	v_add_u32_e32 v6, 0x1400, v6
	s_mov_b32 s0, 0xa800
	v_cndmask_b32_e32 v4, 0, v5, vcc
	v_cmp_ne_u32_e32 vcc, 0, v1
	v_mov_b32_e32 v1, 0x1400
	v_mov_b32_e32 v5, v0
	v_cndmask_b32_e32 v1, v1, v6, vcc
	v_add_u32_e32 v1, v1, v4
	v_min_u32_e32 v4, 0xa800, v1
	v_add_u32_e32 v1, s89, v4
	v_add_u32_e32 v1, v1, v2
	v_cmp_gt_i32_e32 vcc, s0, v1
	s_and_saveexec_b64 s[6:7], vcc
	s_cbranch_execz .LBB0_165
	v_and_b32_e32 v68, 56, v5
	v_and_b32_e32 v5, 7, v5
	v_lshlrev_b32_e32 v6, 2, v5
	v_lshlrev_b32_e32 v8, 12, v5
	v_lshlrev_b32_e32 v4, 5, v4
	v_lshlrev_b32_e32 v69, 15, v1
	v_lshlrev_b32_e32 v80, 1, v1
	v_lshl_add_u32 v81, v2, 5, v4
	v_lshlrev_b32_e32 v82, 8, v1
	s_mov_b64 s[14:15], 0
	v_lshlrev_b32_e32 v70, 2, v6
	v_lshlrev_b32_e32 v72, 1, v68
	v_lshlrev_b32_e32 v74, 1, v8
	s_branch .LBB0_146

; __device__ __forceinline__ void side_range(const Params& p, int layer, int beg, int end, int first, int stride) {
;     ...
;     for (int it0 = beg + first; it0 < end; it0 += 2 * stride) {
;         f32x4 v0[8], v1[8]; const int it1 = it0 + stride; const bool two = it1 < end;
;         moe_item_copy_nt(p, layer, it0, lane, v0, false); if (two) moe_item_copy_nt(p, layer, it1, lane, v1, false);
;         moe_item_copy_nt(p, layer, it0, lane, v0, true); if (two) moe_item_copy_nt(p, layer, it1, lane, v1, true);
;     }
.LBB0_145:
	s_or_b64 exec, exec, s[0:1]
	s_mov_b32 s0, 0x97ff
	v_add_u32_e32 v2, 0x1000, v1
	v_cmp_lt_i32_e32 vcc, s0, v1
	v_add_u32_e32 v69, 0x8000000, v69
	v_add_u32_e32 v80, 0x2000, v80
	v_add_u32_e32 v81, 0x20000, v81
	v_add_u32_e32 v82, 0x100000, v82
	s_or_b64 s[14:15], vcc, s[14:15]
	v_mov_b32_e32 v1, v2
	s_andn2_b64 exec, exec, s[14:15]
	s_cbranch_execz .LBB0_165

; __device__ __forceinline__ void moe_item_copy_nt(const Params& p, int layer, int it, int lane, f32x4 (&v)[8], bool store) {
;     const float* W; int N, k0, nlog0; bf16_t* WT; moe_item_addr(p, layer, it, W, N, WT, k0, nlog0);
;     const int g = lane >> 3, nq = lane & 7;
;     if (!store) {
; #pragma unroll
;         for (int j = 0; j < 8; ++j) v[j] = __builtin_nontemporal_load((const f32x4*)(W + (size_t)(k0 + 8 * g + j) * N + nlog0 + 4 * nq));
; __device__ __forceinline__ void side_range(const Params& p, int layer, int beg, int end, int first, int stride) {
;     ...
;     for (int it0 = beg + first; it0 < end; it0 += 2 * stride) {
;         f32x4 v0[8], v1[8]; const int it1 = it0 + stride; const bool two = it1 < end;
;         moe_item_copy_nt(p, layer, it0, lane, v0, false); if (two) moe_item_copy_nt(p, layer, it1, lane, v1, false);
;         moe_item_copy_nt(p, layer, it0, lane, v0, true); if (two) moe_item_copy_nt(p, layer, it1, lane, v1, true);
.LBB0_150:
	s_or_b64 exec, exec, s[0:1]
	s_movk_i32 s0, 0x3c0
	v_and_or_b32 v61, v38, s0, v68
	v_lshl_add_u64 v[36:37], v[2:3], 2, v[36:37]
	v_mov_b32_e32 v71, v3
	v_mul_u32_u24_e32 v2, v60, v61
	v_lshl_add_u64 v[62:63], v[36:37], 0, v[70:71]
	v_lshlrev_b32_e32 v2, 2, v2
	v_lshl_add_u64 v[36:37], v[62:63], 0, v[2:3]
	v_or_b32_e32 v2, 1, v61
	v_mul_u32_u24_e32 v2, v60, v2
	v_lshlrev_b32_e32 v2, 2, v2
	v_lshl_add_u64 v[40:41], v[62:63], 0, v[2:3]
	v_or_b32_e32 v2, 2, v61
	v_mul_u32_u24_e32 v2, v60, v2
	v_lshlrev_b32_e32 v2, 2, v2
	v_lshl_add_u64 v[44:45], v[62:63], 0, v[2:3]
	v_or_b32_e32 v2, 3, v61
	v_mul_u32_u24_e32 v2, v60, v2
	v_lshlrev_b32_e32 v2, 2, v2
	v_lshl_add_u64 v[48:49], v[62:63], 0, v[2:3]
	v_or_b32_e32 v2, 4, v61
	v_mul_u32_u24_e32 v2, v60, v2
	v_lshlrev_b32_e32 v2, 2, v2
	v_lshl_add_u64 v[52:53], v[62:63], 0, v[2:3]
	v_or_b32_e32 v2, 5, v61
	v_mul_u32_u24_e32 v2, v60, v2
	v_lshlrev_b32_e32 v2, 2, v2
	v_lshl_add_u64 v[56:57], v[62:63], 0, v[2:3]
	v_or_b32_e32 v2, 6, v61
	v_mul_u32_u24_e32 v2, v60, v2
	v_lshlrev_b32_e32 v2, 2, v2
	v_lshl_add_u64 v[64:65], v[62:63], 0, v[2:3]
	v_or_b32_e32 v2, 7, v61
	v_mul_u32_u24_e32 v2, v60, v2
	v_lshlrev_b32_e32 v2, 2, v2
	v_lshl_add_u64 v[66:67], v[62:63], 0, v[2:3]
	global_load_dwordx4 v[36:39], v[36:37], off nt
	s_nop 0
	global_load_dwordx4 v[40:43], v[40:41], off nt
	s_nop 0
	global_load_dwordx4 v[44:47], v[44:45], off nt
	s_nop 0
	global_load_dwordx4 v[48:51], v[48:49], off nt
	s_nop 0
	global_load_dwordx4 v[52:55], v[52:53], off nt
	s_nop 0
	global_load_dwordx4 v[56:59], v[56:57], off nt
	s_nop 0
	global_load_dwordx4 v[60:63], v[64:65], off nt
	s_nop 0
	global_load_dwordx4 v[64:67], v[66:67], off nt
	s_mov_b32 s0, 0xa000
	v_add_u32_e32 v83, 0x800, v1
	v_cmp_gt_i32_e64 s[42:43], s0, v1
	s_and_saveexec_b64 s[4:5], s[42:43]
	s_cbranch_execz .LBB0_156
	s_movk_i32 s0, 0x77ff
	v_cmp_lt_i32_e64 s[0:1], s0, v1
	s_and_saveexec_b64 s[12:13], s[0:1]
	s_xor_b64 s[0:1], exec, s[12:13]
	s_cbranch_execz .LBB0_153
	v_add_u32_e32 v2, 0xffff8800, v1
	v_lshrrev_b32_e32 v2, 9, v2
	v_add_u32_e32 v2, 32, v2
	v_readlane_b32 s44, v251, 31
	v_and_b32_e32 v7, 0x3e0, v75
	v_lshlrev_b64 v[4:5], 22, v[2:3]
	v_readlane_b32 s50, v251, 37
	v_readlane_b32 s51, v251, 38
	v_readlane_b32 s45, v251, 32
	v_readlane_b32 s46, v251, 33
	v_readlane_b32 s47, v251, 34
	v_readlane_b32 s48, v251, 35
	v_readlane_b32 s49, v251, 36
	v_readlane_b32 s52, v251, 39
	v_readlane_b32 s53, v251, 40
	v_readlane_b32 s54, v251, 41
	v_readlane_b32 s55, v251, 42
	v_readlane_b32 s56, v251, 43
	v_readlane_b32 s57, v251, 44
	v_readlane_b32 s58, v251, 45
	v_readlane_b32 s59, v251, 46
	v_lshl_add_u64 v[4:5], s[50:51], 0, v[4:5]
	v_lshlrev_b32_e32 v6, 1, v83
	v_mov_b32_e32 v2, v7

; __device__ __forceinline__ void moe_item_addr(const Params& p, int layer, int it, const float*& W, int& N, bf16_t*& WT, int& k0, int& nlog0) {
;     if (it < 32 * 1024) { const int mi = layer * 32 + (it >> 10), r = it & 1023, kb = r >> 6, n0 = (r & 63) * 32;
;         W = p.in[25] + (size_t)mi * 1024 * 2048; N = 2048; WT = (bf16_t*)(p.ws + ws::WT_UP) + ((size_t)mi * 2048 + n0) * 1024; k0 = kb * 64; nlog0 = upmap(n0); }
;     else { const int j = it - 32 * 1024, mi = layer * 32 + (j >> 9), r = j & 511, kb = r >> 5, n0 = (r & 31) * 32;
;         W = p.in[27] + (size_t)mi * 1024 * 1024; N = 1024; WT = (bf16_t*)(p.ws + ws::WT_DN) + ((size_t)mi * 1024 + n0) * 1024; k0 = kb * 64; nlog0 = n0; }
; }
; __device__ __forceinline__ void moe_item_load(const Params& p, int layer, int it, int lane, f32x4 (&v)[8]) {
;     const float* W; int N, k0, nlog0; bf16_t* WT; moe_item_addr(p, layer, it, W, N, WT, k0, nlog0);
;     const int g = lane >> 3, nq = lane & 7;
; #pragma unroll
;     for (int j = 0; j < 8; ++j) v[j] = *(const f32x4*)(W + (size_t)(k0 + 8 * g + j) * N + nlog0 + 4 * nq);
; }
; __device__ __forceinline__ void moe_item_store(const Params& p, int layer, int it, int lane, const f32x4 (&v)[8]) {
;     const float* W; int N, k0, nlog0; bf16_t* WT; moe_item_addr(p, layer, it, W, N, WT, k0, nlog0);
;     const int g = lane >> 3, nq = lane & 7;
; #pragma unroll
;     for (int i = 0; i < 4; ++i) { v4u o; o.x = pg8::cvt_pk_bf16(v[0][i], v[1][i]); o.y = pg8::cvt_pk_bf16(v[2][i], v[3][i]); o.z = pg8::cvt_pk_bf16(v[4][i], v[5][i]); o.w = pg8::cvt_pk_bf16(v[6][i], v[7][i]);
;         *(v4u*)(WT + (size_t)(4 * nq + i) * 1024 + k0 + 8 * g) = o; }
; }
; __device__ __forceinline__ void moe_item_copy_nt(const Params& p, int layer, int it, int lane, f32x4 (&v)[8], bool store) {
;     const float* W; int N, k0, nlog0; bf16_t* WT; moe_item_addr(p, layer, it, W, N, WT, k0, nlog0);
;     const int g = lane >> 3, nq = lane & 7;
;     if (!store) {
; #pragma unroll
;         for (int j = 0; j < 8; ++j) v[j] = __builtin_nontemporal_load((const f32x4*)(W + (size_t)(k0 + 8 * g + j) * N + nlog0 + 4 * nq));
;     } else {
; #pragma unroll
;         for (int i = 0; i < 4; ++i) { v4u o; o.x = pg8::cvt_pk_bf16(v[0][i], v[1][i]); o.y = pg8::cvt_pk_bf16(v[2][i], v[3][i]); o.z = pg8::cvt_pk_bf16(v[4][i], v[5][i]); o.w = pg8::cvt_pk_bf16(v[6][i], v[7][i]);
.LBB0_1607:
	s_or_b64 exec, exec, s[0:1]
	v_readlane_b32 s86, v254, 60
	v_readlane_b32 s88, v254, 62
	v_readlane_b32 s87, v254, 61
	v_readlane_b32 s20, v255, 8
	s_cmp_gt_u32 s20, 1
	s_cbranch_scc1 .LBB0_1608
	s_cmp_lt_u32 s86, 64
	s_cbranch_scc1 .LBB0_1608
	s_cmp_lg_u32 s88, 0x100
	s_cbranch_scc1 .LBB0_1608
	v_readlane_b32 s0, v251, 37
	v_readlane_b32 s1, v251, 38
	v_readlane_b32 s4, v251, 45
	v_readlane_b32 s5, v251, 46
	v_readfirstlane_b32 s21, v0
	s_lshr_b32 s21, s21, 6
	s_sub_u32 s6, s86, 64
	s_lshl_b32 s6, s6, 3
	s_add_u32 s6, s6, s21
	s_mul_i32 s7, s20, 0xc00
	s_sub_u32 s6, s6, s7
	s_add_u32 s12, s6, 0x3400
	s_add_u32 s13, s12, 0x600
	s_lshr_b32 s62, s12, 9
	s_and_b32 s63, s12, 0x1ff
	s_lshr_b32 s64, s63, 5
	s_and_b32 s63, s63, 31
	s_lshl_b32 s65, s62, 22
	s_lshl_b32 s66, s64, 18
	s_add_u32 s65, s65, s66
	s_lshl_b32 s66, s63, 7
	s_add_u32 s65, s65, s66
	s_add_u32 s65, s65, 0x8000000
	s_add_u32 s54, s0, s65
	s_addc_u32 s55, s1, 0
	s_lshl_b32 s65, s62, 21
	s_lshl_b32 s66, s63, 16
	s_add_u32 s65, s65, s66
	s_lshl_b32 s66, s64, 7
	s_add_u32 s65, s65, s66
	s_add_u32 s65, s65, 0x66881000
	s_add_u32 s56, s4, s65
	s_addc_u32 s57, s5, 0
	s_lshr_b32 s62, s13, 9
	s_and_b32 s63, s13, 0x1ff
	s_lshr_b32 s64, s63, 5
	s_and_b32 s63, s63, 31
	s_lshl_b32 s65, s62, 22
	s_lshl_b32 s66, s64, 18
	s_add_u32 s65, s65, s66
	s_lshl_b32 s66, s63, 7
	s_add_u32 s65, s65, s66
	s_add_u32 s65, s65, 0x8000000
	s_add_u32 s58, s0, s65
	s_addc_u32 s59, s1, 0
	s_lshl_b32 s65, s62, 21
	s_lshl_b32 s66, s63, 16
	s_add_u32 s65, s65, s66
	s_lshl_b32 s66, s64, 7
	s_add_u32 s65, s65, s66
	s_add_u32 s65, s65, 0x66881000
	s_add_u32 s60, s4, s65
	s_addc_u32 s61, s5, 0
	v_and_b32_e32 v1, 63, v0
	v_lshrrev_b32_e32 v2, 3, v1
	v_and_b32_e32 v1, 7, v1
	v_lshlrev_b32_e32 v102, 15, v2
	v_lshl_add_u32 v102, v1, 4, v102
	v_add_u32_e32 v103, 0x1000, v102
	v_add_u32_e32 v104, 0x2000, v102
	v_add_u32_e32 v105, 0x3000, v102
	v_add_u32_e32 v106, 0x4000, v102
	v_add_u32_e32 v107, 0x5000, v102
	v_add_u32_e32 v108, 0x6000, v102
	v_add_u32_e32 v109, 0x7000, v102
	v_lshlrev_b32_e32 v110, 13, v1
	v_lshl_add_u32 v110, v2, 4, v110
	v_add_u32_e32 v111, 0x1000, v110
	global_load_dwordx4 v[112:115], v102, s[54:55] nt
	global_load_dwordx4 v[116:119], v103, s[54:55] nt
	global_load_dwordx4 v[120:123], v104, s[54:55] nt
	global_load_dwordx4 v[124:127], v105, s[54:55] nt
	global_load_dwordx4 v[128:131], v106, s[54:55] nt
	global_load_dwordx4 v[132:135], v107, s[54:55] nt
	global_load_dwordx4 v[136:139], v108, s[54:55] nt
	global_load_dwordx4 v[140:143], v109, s[54:55] nt
	global_load_dwordx4 v[216:219], v102, s[58:59] nt
	global_load_dwordx4 v[220:223], v103, s[58:59] nt
	global_load_dwordx4 v[224:227], v104, s[58:59] nt
	global_load_dwordx4 v[228:231], v105, s[58:59] nt
	global_load_dwordx4 v[232:235], v106, s[58:59] nt
	global_load_dwordx4 v[236:239], v107, s[58:59] nt
	global_load_dwordx4 v[240:243], v108, s[58:59] nt
	global_load_dwordx4 v[244:247], v109, s[58:59] nt
	s_waitcnt vmcnt(8)
	v_cvt_pk_bf16_f32 v144, v112, v116
	v_cvt_pk_bf16_f32 v145, v120, v124
	v_cvt_pk_bf16_f32 v146, v128, v132
	v_cvt_pk_bf16_f32 v147, v136, v140
	v_cvt_pk_bf16_f32 v148, v113, v117
	v_cvt_pk_bf16_f32 v149, v121, v125
	v_cvt_pk_bf16_f32 v150, v129, v133
	v_cvt_pk_bf16_f32 v151, v137, v141
	v_cvt_pk_bf16_f32 v152, v114, v118
	v_cvt_pk_bf16_f32 v153, v122, v126
	v_cvt_pk_bf16_f32 v154, v130, v134
	v_cvt_pk_bf16_f32 v155, v138, v142
	v_cvt_pk_bf16_f32 v156, v115, v119
	v_cvt_pk_bf16_f32 v157, v123, v127
	v_cvt_pk_bf16_f32 v158, v131, v135
	v_cvt_pk_bf16_f32 v159, v139, v143
	global_store_dwordx4 v110, v[144:147], s[56:57] nt
	global_store_dwordx4 v110, v[148:151], s[56:57] offset:2048 nt
	global_store_dwordx4 v111, v[152:155], s[56:57] nt
	global_store_dwordx4 v111, v[156:159], s[56:57] offset:2048 nt
	s_waitcnt vmcnt(4)
	v_cvt_pk_bf16_f32 v178, v216, v220
	v_cvt_pk_bf16_f32 v179, v224, v228
	v_cvt_pk_bf16_f32 v180, v232, v236
	v_cvt_pk_bf16_f32 v181, v240, v244
	v_cvt_pk_bf16_f32 v182, v217, v221
	v_cvt_pk_bf16_f32 v183, v225, v229
	v_cvt_pk_bf16_f32 v184, v233, v237
	v_cvt_pk_bf16_f32 v185, v241, v245
	v_cvt_pk_bf16_f32 v186, v218, v222
	v_cvt_pk_bf16_f32 v187, v226, v230
	v_cvt_pk_bf16_f32 v188, v234, v238
	v_cvt_pk_bf16_f32 v189, v242, v246
	v_cvt_pk_bf16_f32 v190, v219, v223
	v_cvt_pk_bf16_f32 v191, v227, v231
	v_cvt_pk_bf16_f32 v192, v235, v239
	v_cvt_pk_bf16_f32 v193, v243, v247
	global_store_dwordx4 v110, v[178:181], s[60:61] nt
	global_store_dwordx4 v110, v[182:185], s[60:61] offset:2048 nt
	global_store_dwordx4 v111, v[186:189], s[60:61] nt
	global_store_dwordx4 v111, v[190:193], s[60:61] offset:2048 nt

; __device__ __forceinline__ int otid() { int t = threadIdx.x; asm volatile("" : "+v"(t)); return t; }
; #pragma unroll
;     for (int e = 0; e < 32; ++e) t += (cnt[e] + 255) >> 8;
;     return t; }
; __device__ __forceinline__ void side_range(const Params& p, int layer, int beg, int end, int first, int stride) {
;     const int lane = otid() & 63;
; #pragma unroll 1
;     for (int it0 = beg + first; it0 < end; it0 += 2 * stride) {
;         f32x4 v0[8], v1[8]; const int it1 = it0 + stride; const bool two = it1 < end;
;         moe_item_copy_nt(p, layer, it0, lane, v0, false); if (two) moe_item_copy_nt(p, layer, it1, lane, v1, false);
;         moe_item_copy_nt(p, layer, it0, lane, v0, true); if (two) moe_item_copy_nt(p, layer, it1, lane, v1, true);
;     }
; }
; __device__ __forceinline__ PoolRanges pool_ranges(const Params& p, int L) {
;     const int T = moe_tiles((const int*)(p.ws + ws::CTL) + ws::CW_CNT + L * 32);
;     PoolRanges r; r.rem_up = (8 * T) & 255; r.ns_up = r.rem_up ? 256 - r.rem_up : 0; r.rem_dn = T & 63; r.ns_dn = r.rem_dn ? (64 - r.rem_dn) * 4 : 0;
;     r.beg_up = L == 0 ? POOL1_BEG : (L == 1 ? POOL2_BEG : POOL3_BEG); r.pool_end = L == 0 ? 49152 : (L == 1 ? POOL2_END : POOL3_END);
;     r.end_up = min(r.beg_up + r.ns_up * 8 * SIDE_JU, r.pool_end); r.end_dn = min(r.end_up + r.ns_dn * 8 * SIDE_JU, r.pool_end);
;     return r;
; }
; __device__ __forceinline__ void moe_up_tail(const Params& p, int L, int bid) {
;     const PoolRanges r = pool_ranges(p, L);
;     if (r.ns_up && bid >= r.rem_up) side_range(p, L + 1, r.beg_up, r.end_up, (bid - r.rem_up) * 8 + (otid() >> 6), r.ns_up * 8);
; }
.LBB0_1724:
	v_readlane_b32 s0, v255, 8
	v_readlane_b32 s1, v255, 9
	s_cmp_eq_u32 s0, 3
	v_readlane_b32 s4, v254, 58
	s_cselect_b64 s[0:1], -1, 0
	v_readlane_b32 s5, v254, 59
	s_or_b64 s[0:1], s[4:5], s[0:1]
	v_readlane_b32 s26, v250, 23
	s_and_b64 vcc, exec, s[0:1]
	v_readlane_b32 s27, v250, 24
	s_cbranch_vccnz .LBB0_1750
	s_lshl_b64 s[0:1], s[30:31], 2
	v_readlane_b32 s4, v249, 56
	v_readlane_b32 s5, v249, 57
	s_add_u32 s0, s4, s0
	s_addc_u32 s1, s5, s1
	global_load_dwordx4 v[4:7], v3, s[0:1] offset:48
	global_load_dwordx4 v[8:11], v3, s[0:1] offset:32
	global_load_dwordx4 v[12:15], v3, s[0:1] offset:16
	global_load_dwordx4 v[16:19], v3, s[0:1]
	s_waitcnt vmcnt(0)
	v_add_u32_e32 v1, 0xff, v16
	v_add_u32_e32 v2, 0xff, v17
	v_ashrrev_i32_e32 v1, 8, v1
	v_ashrrev_i32_e32 v2, 8, v2
	v_add_u32_e32 v1, v2, v1
	v_add_u32_e32 v2, 0xff, v18
	v_ashrrev_i32_e32 v2, 8, v2
	v_add_u32_e32 v1, v1, v2
	v_add_u32_e32 v2, 0xff, v19
	v_ashrrev_i32_e32 v2, 8, v2
	v_add_u32_e32 v1, v1, v2
	v_add_u32_e32 v2, 0xff, v12
	v_ashrrev_i32_e32 v2, 8, v2
	v_add_u32_e32 v1, v1, v2
	v_add_u32_e32 v2, 0xff, v13
	v_ashrrev_i32_e32 v2, 8, v2
	v_add_u32_e32 v1, v1, v2
	v_add_u32_e32 v2, 0xff, v14
	v_ashrrev_i32_e32 v2, 8, v2
	v_add_u32_e32 v1, v1, v2
	v_add_u32_e32 v2, 0xff, v15
	v_ashrrev_i32_e32 v2, 8, v2
	v_add_u32_e32 v1, v1, v2
	v_add_u32_e32 v2, 0xff, v8
	v_ashrrev_i32_e32 v2, 8, v2
	v_add_u32_e32 v1, v1, v2
	v_add_u32_e32 v2, 0xff, v9
	v_ashrrev_i32_e32 v2, 8, v2
	v_add_u32_e32 v1, v1, v2
	v_add_u32_e32 v2, 0xff, v10
	v_ashrrev_i32_e32 v2, 8, v2
	v_add_u32_e32 v1, v1, v2
	v_add_u32_e32 v2, 0xff, v11
	v_ashrrev_i32_e32 v2, 8, v2
	v_add_u32_e32 v1, v1, v2
	v_add_u32_e32 v2, 0xff, v4
	v_ashrrev_i32_e32 v2, 8, v2
	v_add_u32_e32 v1, v1, v2
	v_add_u32_e32 v2, 0xff, v5
	v_ashrrev_i32_e32 v2, 8, v2
	v_add_u32_e32 v1, v1, v2
	v_add_u32_e32 v2, 0xff, v6
	v_ashrrev_i32_e32 v2, 8, v2
	v_add_u32_e32 v1, v1, v2
	v_add_u32_e32 v2, 0xff, v7
	global_load_dwordx4 v[4:7], v3, s[0:1] offset:112
	global_load_dwordx4 v[8:11], v3, s[0:1] offset:96
	global_load_dwordx4 v[12:15], v3, s[0:1] offset:80
	global_load_dwordx4 v[16:19], v3, s[0:1] offset:64
	v_ashrrev_i32_e32 v2, 8, v2
	v_add_u32_e32 v1, v1, v2
	s_waitcnt vmcnt(0)
	v_add_u32_e32 v2, 0xff, v16
	v_ashrrev_i32_e32 v2, 8, v2
	v_add_u32_e32 v1, v1, v2
	v_add_u32_e32 v2, 0xff, v17
	v_ashrrev_i32_e32 v2, 8, v2
	v_add_u32_e32 v1, v1, v2
	v_add_u32_e32 v2, 0xff, v18
	v_ashrrev_i32_e32 v2, 8, v2
	v_add_u32_e32 v1, v1, v2
	v_add_u32_e32 v2, 0xff, v19
	v_ashrrev_i32_e32 v2, 8, v2
	v_add_u32_e32 v1, v1, v2
	v_add_u32_e32 v2, 0xff, v12
	v_ashrrev_i32_e32 v2, 8, v2
	v_add_u32_e32 v1, v1, v2
	v_add_u32_e32 v2, 0xff, v13
	v_ashrrev_i32_e32 v2, 8, v2
	v_add_u32_e32 v1, v1, v2
	v_add_u32_e32 v2, 0xff, v14
	v_add_u32_e32 v12, 0xff, v15
	v_ashrrev_i32_e32 v2, 8, v2
	v_ashrrev_i32_e32 v12, 8, v12
	v_add_u32_e32 v1, v1, v2
	v_add_u32_e32 v2, 0xff, v8
	v_add_u32_e32 v1, v1, v12
	v_add_u32_e32 v8, 0xff, v9
	v_ashrrev_i32_e32 v2, 8, v2
	v_ashrrev_i32_e32 v8, 8, v8
	v_add_u32_e32 v1, v1, v2
	v_add_u32_e32 v2, 0xff, v10
	v_add_u32_e32 v1, v1, v8
	v_add_u32_e32 v8, 0xff, v11
	v_ashrrev_i32_e32 v2, 8, v2
	v_ashrrev_i32_e32 v8, 8, v8
	v_add_u32_e32 v1, v1, v2
	v_add_u32_e32 v2, 0xff, v4
	v_add_u32_e32 v1, v1, v8
	v_add_u32_e32 v4, 0xff, v5
	v_ashrrev_i32_e32 v2, 8, v2
	v_ashrrev_i32_e32 v4, 8, v4
	v_add_u32_e32 v1, v1, v2
	v_add_u32_e32 v2, 0xff, v6
	v_add_u32_e32 v1, v1, v4
	v_add_u32_e32 v4, 0xff, v7
	v_ashrrev_i32_e32 v2, 8, v2
	v_ashrrev_i32_e32 v4, 8, v4
	v_add_u32_e32 v1, v1, v2
	v_add_u32_e32 v2, v1, v4
	v_lshlrev_b32_e32 v1, 3, v2
	v_and_b32_e32 v4, 0xf8, v1
	v_cmp_eq_u32_e64 s[0:1], 0, v4
	v_cmp_lt_i32_e32 vcc, s86, v4
	s_or_b64 s[4:5], s[0:1], vcc
	s_and_b64 vcc, exec, s[4:5]
	s_cbranch_vccnz .LBB0_1750
	v_readlane_b32 s4, v255, 8
	v_readlane_b32 s5, v255, 9
	s_mov_b32 s6, s4
	s_cmp_eq_u32 s4, 1
	s_movk_i32 s4, 0x5c00
	s_mov_b32 s5, 0xa000
	s_cselect_b32 s4, s4, 0x9000
	s_cselect_b32 s5, s5, 0xb000
	s_cmp_eq_u32 s6, 0
	v_sub_u32_e32 v5, 0x100, v4
	s_movk_i32 s6, 0x60
	v_sub_u32_e32 v4, s86, v4
	v_mul_lo_u32 v1, v5, s6
	v_lshlrev_b32_e32 v7, 3, v4
	v_mov_b32_e32 v4, v0
	s_cselect_b32 s4, 0x1400, s4
	v_cndmask_b32_e64 v1, v1, 0, s[0:1]
	s_cselect_b32 s5, 0xa800, s5
	v_add_u32_e32 v1, s4, v1
	v_ashrrev_i32_e32 v4, 6, v4
	v_add_u32_e32 v7, s4, v7
	v_min_u32_e32 v1, s5, v1
	v_add_u32_e32 v69, v7, v4
	v_mov_b32_e32 v6, v0
	v_cmp_lt_i32_e32 vcc, v69, v1
	s_and_saveexec_b64 s[6:7], vcc
	s_cbranch_execz .LBB0_1749
	v_and_b32_e32 v7, 7, v6
	v_and_b32_e32 v2, 31, v2
	v_lshlrev_b32_e32 v80, 3, v5
	v_and_b32_e32 v68, 56, v6
	v_lshlrev_b32_e32 v6, 2, v7
	v_lshlrev_b32_e32 v8, 12, v7
	v_lshlrev_b32_e32 v81, 4, v5
	v_add_u32_e32 v5, s4, v4
	v_lshlrev_b32_e32 v7, 6, v2
	v_sub_u32_e32 v82, v5, v7
	v_lshlrev_b32_e32 v7, 22, v2
	v_sub_u32_e32 v84, 0x8000000, v7
	s_lshl_b32 s0, s4, 1
	v_lshlrev_b32_e32 v7, 1, v4
	s_lshl_b32 s1, s4, 5
	v_readlane_b32 s4, v251, 17
	v_add_u32_e32 v9, s0, v7
	v_lshlrev_b32_e32 v10, 7, v2
	s_add_i32 s1, s4, s1
	v_sub_u32_e32 v85, v9, v10
	v_lshlrev_b32_e32 v9, 8, v2
	v_lshlrev_b32_e32 v11, 11, v2
	v_lshl_add_u32 v88, v4, 5, s1
	v_lshlrev_b32_e32 v4, 12, v2
	v_lshlrev_b32_e32 v2, 15, v2
	s_addk_i32 s0, 0x1000
	v_sub_u32_e32 v91, 0x100000, v2
	v_add_u32_e32 v2, s0, v7
	s_add_i32 s8, s30, 32
	v_lshlrev_b32_e32 v83, 15, v69
	v_sub_u32_e32 v86, 0x2000, v9
	v_sub_u32_e32 v87, 0, v11
	v_sub_u32_e32 v89, 0x20000, v4
	v_lshlrev_b32_e32 v90, 8, v69
	v_sub_u32_e32 v92, v5, v10
	v_sub_u32_e32 v93, v2, v9
	v_sub_u32_e32 v94, 0x10000, v4
	s_mov_b64 s[14:15], 0
	v_lshlrev_b32_e32 v70, 2, v6
	v_lshlrev_b32_e32 v72, 1, v68
	v_lshlrev_b32_e32 v74, 1, v8
	s_branch .LBB0_1730

; __device__ __forceinline__ int otid() { int t = threadIdx.x; asm volatile("" : "+v"(t)); return t; }
; #pragma unroll
;     for (int e = 0; e < 32; ++e) t += (cnt[e] + 255) >> 8;
;     return t; }
; __device__ __forceinline__ void side_range(const Params& p, int layer, int beg, int end, int first, int stride) {
;     const int lane = otid() & 63;
; #pragma unroll 1
;     for (int it0 = beg + first; it0 < end; it0 += 2 * stride) {
;         f32x4 v0[8], v1[8]; const int it1 = it0 + stride; const bool two = it1 < end;
;         moe_item_copy_nt(p, layer, it0, lane, v0, false); if (two) moe_item_copy_nt(p, layer, it1, lane, v1, false);
;         moe_item_copy_nt(p, layer, it0, lane, v0, true); if (two) moe_item_copy_nt(p, layer, it1, lane, v1, true);
;     }
; }
; __device__ __forceinline__ PoolRanges pool_ranges(const Params& p, int L) {
;     const int T = moe_tiles((const int*)(p.ws + ws::CTL) + ws::CW_CNT + L * 32);
;     PoolRanges r; r.rem_up = (8 * T) & 255; r.ns_up = r.rem_up ? 256 - r.rem_up : 0; r.rem_dn = T & 63; r.ns_dn = r.rem_dn ? (64 - r.rem_dn) * 4 : 0;
;     r.beg_up = L == 0 ? POOL1_BEG : (L == 1 ? POOL2_BEG : POOL3_BEG); r.pool_end = L == 0 ? 49152 : (L == 1 ? POOL2_END : POOL3_END);
;     r.end_up = min(r.beg_up + r.ns_up * 8 * SIDE_JU, r.pool_end); r.end_dn = min(r.end_up + r.ns_dn * 8 * SIDE_JU, r.pool_end);
;     return r;
; }
; __device__ __forceinline__ void moe_up_tail(const Params& p, int L, int bid) {
;     const PoolRanges r = pool_ranges(p, L);
;     if (r.ns_up && bid >= r.rem_up) side_range(p, L + 1, r.beg_up, r.end_up, (bid - r.rem_up) * 8 + (otid() >> 6), r.ns_up * 8);
; }
; __device__ __forceinline__ void moe_down_tail(const Params& p, int L, int bid) {
;     const PoolRanges r = pool_ranges(p, L); const int j = bid >> 3, tl = (bid & 7) * 8 + (j >> 2);
;     if (r.ns_dn && tl >= r.rem_dn) side_range(p, L + 1, r.end_up, r.end_dn, ((tl - r.rem_dn) * 4 + (j & 3)) * 8 + (otid() >> 6), r.ns_dn * 8);
; }
.LBB0_1824:
	v_readlane_b32 s0, v255, 8
	v_readlane_b32 s1, v255, 9
	s_cmp_eq_u32 s0, 3
	v_readlane_b32 s4, v254, 58
	s_cselect_b64 s[0:1], -1, 0
	v_readlane_b32 s5, v254, 59
	s_or_b64 s[0:1], s[4:5], s[0:1]
	s_and_b64 vcc, exec, s[0:1]
	s_cbranch_vccnz .LBB0_1851
	s_lshl_b64 s[0:1], s[30:31], 2
	v_readlane_b32 s4, v249, 56
	v_readlane_b32 s5, v249, 57
	s_add_u32 s0, s4, s0
	s_addc_u32 s1, s5, s1
	global_load_dwordx4 v[4:7], v3, s[0:1] offset:48
	global_load_dwordx4 v[8:11], v3, s[0:1] offset:32
	global_load_dwordx4 v[12:15], v3, s[0:1] offset:16
	global_load_dwordx4 v[16:19], v3, s[0:1]
	global_load_dwordx4 v[20:23], v3, s[0:1] offset:112
	global_load_dwordx4 v[24:27], v3, s[0:1] offset:96
	global_load_dwordx4 v[28:31], v3, s[0:1] offset:80
	global_load_dwordx4 v[32:35], v3, s[0:1] offset:64
	s_waitcnt vmcnt(0)
	v_readfirstlane_b32 s4, v7
	v_readfirstlane_b32 s5, v6
	v_readfirstlane_b32 s6, v5
	v_readfirstlane_b32 s7, v4
	s_addk_i32 s7, 0xff
	s_ashr_i32 s7, s7, 8
	s_addk_i32 s6, 0xff
	s_ashr_i32 s6, s6, 8
	s_addk_i32 s5, 0xff
	s_ashr_i32 s5, s5, 8
	s_addk_i32 s4, 0xff
	s_ashr_i32 s4, s4, 8
	v_readfirstlane_b32 s8, v11
	v_readfirstlane_b32 s12, v10
	v_readfirstlane_b32 s13, v9
	v_readfirstlane_b32 s14, v8
	s_addk_i32 s14, 0xff
	s_ashr_i32 s14, s14, 8
	s_addk_i32 s13, 0xff
	s_ashr_i32 s13, s13, 8
	s_addk_i32 s12, 0xff
	s_ashr_i32 s12, s12, 8
	s_addk_i32 s8, 0xff
	s_ashr_i32 s8, s8, 8
	v_readfirstlane_b32 s15, v15
	v_readfirstlane_b32 s16, v14
	v_readfirstlane_b32 s17, v13
	v_readfirstlane_b32 s20, v12
	s_addk_i32 s20, 0xff
	s_ashr_i32 s20, s20, 8
	s_addk_i32 s17, 0xff
	s_ashr_i32 s17, s17, 8
	s_addk_i32 s16, 0xff
	s_ashr_i32 s16, s16, 8
	s_addk_i32 s15, 0xff
	s_ashr_i32 s15, s15, 8
	v_readfirstlane_b32 s21, v19
	v_readfirstlane_b32 s22, v18
	v_readfirstlane_b32 s23, v17
	v_readfirstlane_b32 s24, v16
	s_addk_i32 s24, 0xff
	s_addk_i32 s23, 0xff
	s_ashr_i32 s24, s24, 8
	s_ashr_i32 s23, s23, 8
	s_addk_i32 s22, 0xff
	s_add_i32 s23, s23, s24
	s_ashr_i32 s22, s22, 8
	s_addk_i32 s21, 0xff
	s_add_i32 s22, s23, s22
	s_ashr_i32 s21, s21, 8
	s_add_i32 s21, s22, s21
	s_add_i32 s20, s21, s20
	s_add_i32 s17, s20, s17
	s_add_i32 s16, s17, s16
	s_add_i32 s15, s16, s15
	s_add_i32 s14, s15, s14
	s_add_i32 s13, s14, s13
	s_add_i32 s12, s13, s12
	s_add_i32 s8, s12, s8
	s_add_i32 s7, s8, s7
	s_add_i32 s6, s7, s6
	s_add_i32 s8, s6, s5
	s_add_i32 s8, s8, s4
	v_readfirstlane_b32 s4, v23
	v_readfirstlane_b32 s5, v22
	v_readfirstlane_b32 s6, v21
	v_readfirstlane_b32 s7, v20
	s_addk_i32 s7, 0xff
	s_addk_i32 s6, 0xff
	s_addk_i32 s5, 0xff
	s_addk_i32 s4, 0xff
	v_readfirstlane_b32 s12, v27
	v_readfirstlane_b32 s13, v26
	v_readfirstlane_b32 s14, v25
	v_readfirstlane_b32 s15, v24
	s_addk_i32 s15, 0xff
	s_addk_i32 s14, 0xff
	s_addk_i32 s13, 0xff
	s_addk_i32 s12, 0xff
	v_readfirstlane_b32 s16, v31
	v_readfirstlane_b32 s17, v30
	v_readfirstlane_b32 s22, v29
	v_readfirstlane_b32 s23, v28
	s_addk_i32 s23, 0xff
	s_addk_i32 s22, 0xff
	s_addk_i32 s17, 0xff
	s_addk_i32 s16, 0xff
	v_readfirstlane_b32 s21, v32
	v_readfirstlane_b32 s20, v33
	s_addk_i32 s21, 0xff
	v_readfirstlane_b32 s1, v34
	s_ashr_i32 s21, s21, 8
	s_addk_i32 s20, 0xff
	v_readfirstlane_b32 s0, v35
	s_add_i32 s8, s8, s21
	s_ashr_i32 s20, s20, 8
	s_addk_i32 s1, 0xff
	s_add_i32 s8, s8, s20
	s_ashr_i32 s1, s1, 8
	s_addk_i32 s0, 0xff
	s_add_i32 s1, s8, s1
	s_ashr_i32 s0, s0, 8
	s_add_i32 s0, s1, s0
	s_ashr_i32 s8, s23, 8
	s_ashr_i32 s1, s22, 8
	s_add_i32 s0, s0, s8
	s_add_i32 s0, s0, s1
	s_ashr_i32 s8, s17, 8
	s_ashr_i32 s1, s16, 8
	s_add_i32 s0, s0, s8
	s_add_i32 s0, s0, s1
	s_ashr_i32 s8, s15, 8
	s_ashr_i32 s1, s14, 8
	s_add_i32 s0, s0, s8
	s_add_i32 s0, s0, s1
	s_ashr_i32 s8, s13, 8
	s_ashr_i32 s1, s12, 8
	s_add_i32 s0, s0, s8
	s_add_i32 s0, s0, s1
	s_ashr_i32 s1, s6, 8
	s_ashr_i32 s6, s7, 8
	s_add_i32 s0, s0, s6
	s_add_i32 s0, s0, s1
	s_ashr_i32 s1, s4, 8
	s_ashr_i32 s4, s5, 8
	s_add_i32 s5, s0, s4
	s_add_i32 s5, s5, s1
	s_and_b32 s4, s5, 63
	s_cmp_eq_u32 s4, 0
	v_readlane_b32 s6, v251, 10
	s_cselect_b64 s[0:1], -1, 0
	s_cmp_lt_i32 s6, s4
	s_cselect_b64 s[6:7], -1, 0
	s_or_b64 s[6:7], s[0:1], s[6:7]
	s_and_b64 vcc, exec, s[6:7]
	s_cbranch_vccnz .LBB0_1850
	s_lshl_b32 s6, s4, 2
	s_sub_i32 s14, 0x100, s6
	v_readlane_b32 s6, v255, 8
	v_readlane_b32 s7, v255, 9
	s_mov_b32 s8, s6
	s_cmp_eq_u32 s6, 1
	s_movk_i32 s6, 0x5c00
	s_mov_b32 s7, 0xa000
	s_cselect_b32 s6, s6, 0x9000
	s_cselect_b32 s7, s7, 0xb000
	s_cmp_eq_u32 s8, 0
	s_cselect_b32 s6, 0x1400, s6
	s_cselect_b32 s7, 0xa800, s7
	s_lshl_b32 s5, s5, 3
	s_and_b32 s5, s5, 0xf8
	s_sub_i32 s8, 0x100, s5
	s_mulk_i32 s8, 0x60
	s_cmp_lg_u32 s5, 0
	s_cselect_b32 s5, s8, 0
	s_add_i32 s5, s5, s6
	s_min_u32 s5, s5, s7
	s_mul_i32 s6, s14, 0x60
	s_and_b64 s[0:1], s[0:1], exec
	s_cselect_b32 s0, 0, s6
	s_add_i32 s0, s5, s0
	s_min_u32 s8, s0, s7
	v_readlane_b32 s0, v251, 10
	s_sub_i32 s0, s0, s4
	s_lshl_b32 s1, s0, 5
	v_readlane_b32 s21, v251, 12
	s_or_b32 s6, s1, s21
	v_mov_b32_e32 v1, v0
	s_add_i32 s6, s6, s5
	v_ashrrev_i32_e32 v2, 6, v1
	v_add_u32_e32 v1, s6, v2
	v_mov_b32_e32 v4, v0
	v_cmp_gt_i32_e32 vcc, s8, v1
	s_and_saveexec_b64 s[6:7], vcc
	s_cbranch_execz .LBB0_1849
	v_and_b32_e32 v5, 7, v4
	v_and_b32_e32 v68, 56, v4
	v_lshlrev_b32_e32 v4, 2, v5
	v_lshlrev_b32_e32 v6, 12, v5
	v_add_u32_e32 v5, s5, v2
	s_lshl_b32 s12, s14, 3
	s_lshl_b32 s16, s14, 4
	v_add_u32_e32 v69, s1, v5
	s_lshl_b32 s1, s4, 20
	v_readlane_b32 s14, v251, 55
	s_sub_i32 s1, s14, s1
	v_readlane_b32 s15, v251, 47
	s_lshl_b32 s14, s5, 15
	s_add_i32 s22, s15, s1
	s_lshl_b32 s1, s0, 6
	s_lshl_b32 s15, s5, 1
	s_lshl_b32 s0, s0, 10
	s_lshl_b32 s5, s5, 5
	s_lshl_b32 s20, s4, 14
	v_lshl_add_u32 v80, v2, 15, s14
	v_lshlrev_b32_e32 v7, 1, v2
	s_add_i32 s1, s15, s1
	v_lshlrev_b32_e32 v2, 5, v2
	s_add_i32 s0, s5, s0
	s_sub_i32 s25, 0x100000, s20
	v_readlane_b32 s20, v251, 48
	s_lshl_b32 s14, s4, 21
	v_add_u32_e32 v81, s1, v7
	s_lshl_b32 s1, s4, 7
	v_add_u32_e32 v82, s0, v2
	s_lshl_b32 s0, s4, 11
	v_add_u32_e32 v5, s20, v5
	s_lshl_b32 s20, s4, 5
	s_lshl_b32 s4, s4, 6
	v_subrev_u32_e32 v85, s4, v5
	v_readlane_b32 s4, v251, 56
	v_subrev_u32_e32 v84, s20, v5
	s_sub_i32 s23, 0x2000, s1
	v_add_u32_e32 v5, s4, v80
	v_readlane_b32 s4, v251, 51
	s_add_i32 s15, s15, s4
	v_subrev_u32_e32 v86, s14, v5
	v_add_u32_e32 v5, s15, v7
	v_subrev_u32_e32 v87, s1, v5
	v_readlane_b32 s1, v251, 52
	s_add_i32 s5, s5, s1
	v_add_u32_e32 v2, s5, v2
	s_add_i32 s13, s30, 32
	s_sub_i32 s17, 0x8000000, s14
	s_sub_i32 s24, 0x20000, s0
	v_lshlrev_b32_e32 v83, 8, v1
	v_subrev_u32_e32 v88, s0, v2
	s_mov_b64 s[14:15], 0
	v_lshlrev_b32_e32 v70, 2, v4
	v_lshlrev_b32_e32 v72, 1, v68
	v_lshlrev_b32_e32 v74, 1, v6
	s_branch .LBB0_1830
